# grid barrier generation math specialised for single use (no integer divisions on arrival path)
# baseline (speedup 1.0000x reference)
.LBB2_303:
	s_or_b64 exec, exec, s[12:13]
	s_waitcnt vmcnt(0)
	v_readfirstlane_b32 s10, v5
	s_nop 1
	v_add_u32_e32 v7, s10, v3
	v_mov_b32_e32 v3, 0
	v_add_u32_e32 v5, 1, v7
	v_cmp_ne_u32_e32 vcc, v5, v4
	s_and_saveexec_b64 s[10:11], vcc
	s_xor_b64 s[10:11], exec, s[10:11]
	s_cbranch_execz .LBB2_317
	s_waitcnt lgkmcnt(0)
	v_mov_b32_e32 v2, 0x3500
	global_load_dword v2, v2, s[54:55] sc1
	s_add_u32 s14, s54, 0x3500
	s_addc_u32 s15, s55, 0
	s_waitcnt vmcnt(0)
	v_cmp_eq_u32_e32 vcc, v2, v3
	s_and_saveexec_b64 s[12:13], vcc
	s_cbranch_execz .LBB2_316
	s_mov_b32 s26, 1
	s_mov_b64 s[16:17], 0
	v_mov_b32_e32 v2, 0
	s_branch .LBB2_307

.LBB2_320:
	s_or_b64 exec, exec, s[12:13]
	s_waitcnt vmcnt(0)
	v_readfirstlane_b32 s10, v4
	s_add_u32 s12, s54, 0x3500
	s_addc_u32 s13, s55, 0
	v_add_u32_e32 v3, s10, v3
	v_add_u32_e32 v6, 1, v3
	s_mov_b64 s[14:15], -1
	v_mov_b32_e32 v4, 0
	v_cmp_ne_u32_e32 vcc, v6, v2
	v_mov_b64_e32 v[2:3], s[12:13]
	s_and_saveexec_b64 s[10:11], vcc
	s_cbranch_execz .LBB2_332
	v_mov_b32_e32 v2, 0
	global_load_dword v3, v2, s[12:13] sc1
	s_mov_b64 s[18:19], 0
	s_waitcnt vmcnt(0)
	v_cmp_eq_u32_e32 vcc, v3, v4
	s_and_saveexec_b64 s[16:17], vcc
	s_cbranch_execz .LBB2_331
	s_add_u32 s14, s54, 0x200
	s_addc_u32 s15, s55, 0
	s_mov_b32 s28, 1
	s_branch .LBB2_324
